# baseline (speedup 1.0000x reference)
_Z11prep_kernelPKfS0_PKiPDF16_S3_PfS4_:
	s_lshl_b32 s14, s2, 2
	v_lshrrev_b32_e32 v1, 8, v0
	v_or_b32_e32 v5, s14, v1
	s_movk_i32 s2, 0xff
	v_and_b32_e32 v4, 0xff, v0
	v_cmp_lt_i32_e32 vcc, s2, v5
	s_and_saveexec_b64 s[2:3], vcc
	s_xor_b64 s[2:3], exec, s[2:3]
	s_cbranch_execz .LBB0_5
	v_readfirstlane_b32 s15, v0
	s_bitcmp1_b32 s15, 7
	s_cbranch_scc0 .Lprep_conv
	s_cmpk_gt_u32 s15, 0xff
	s_cbranch_scc1 .LBB0_7
	s_lshr_b32 s16, s14, 2
	s_sub_u32 s16, s16, 64
	s_lshr_b32 s17, s16, 1
	v_mov_b32_e32 v5, s17
	s_and_b32 s16, s16, 1
	s_lshl_b32 s16, s16, 7
	v_and_b32_e32 v4, 0x7f, v0
	v_or_b32_e32 v4, s16, v4
	s_branch .Lprep_rope
.Lprep_conv:
	s_load_dwordx4 s[8:11], s[0:1], 0x0
	s_load_dwordx4 s[4:7], s[0:1], 0x18
	v_add_u32_e32 v34, 0xffffff00, v5
	v_mov_b32_e32 v35, 0
	v_lshlrev_b64 v[32:33], 11, v[34:35]
	v_lshl_or_b32 v32, v4, 3, v32
	v_lshlrev_b64 v[0:1], 2, v[32:33]
	s_waitcnt lgkmcnt(0)
	s_cmp_lg_u32 s14, 0x100
	s_cbranch_scc1 .Lprep_noflag
	s_cmp_gt_u32 s15, 63
	s_cbranch_scc1 .Lprep_noflag
	s_add_u32 s16, s4, 0x3c08000
	s_addc_u32 s17, s5, 0
	v_lshlrev_b32_e32 v6, 2, v4
	v_mov_b32_e32 v7, 0
	v_mov_b32_e32 v8, s8
	v_mov_b32_e32 v9, s9
	v_mov_b32_e32 v10, s10
	v_mov_b32_e32 v11, s11
	global_store_dword v6, v7, s[16:17]
	global_store_dword v6, v7, s[16:17] offset:256
	global_store_dword v6, v7, s[16:17] offset:512
	global_store_dword v6, v7, s[16:17] offset:768
	global_store_dwordx4 v7, v[8:11], s[16:17] offset:1024

.LBB0_3:
	v_lshlrev_b64 v[36:37], 1, v[32:33]
	v_lshl_add_u64 v[38:39], s[4:5], 0, v[36:37]
	s_mov_b32 s4, 0x800000
	s_waitcnt vmcnt(4)
	v_cvt_pk_f16_f32 v28, v28, v29
	v_cvt_pk_f16_f32 v29, v30, v31
	v_cvt_pk_f16_f32 v31, v22, v23
	s_waitcnt vmcnt(2)
	v_cvt_pk_f16_f32 v22, v16, v17
	v_add_co_u32_e32 v16, vcc, s4, v38
	v_cvt_pk_f16_f32 v30, v20, v21
	s_nop 0
	v_addc_co_u32_e32 v17, vcc, 0, v39, vcc
	v_cvt_pk_f16_f32 v20, v24, v25
	v_cvt_pk_f16_f32 v21, v26, v27
	v_cvt_pk_f16_f32 v23, v18, v19
	s_waitcnt vmcnt(0)
	v_cvt_pk_f16_f32 v8, v8, v9
	v_cvt_pk_f16_f32 v9, v10, v11
	v_cvt_pk_f16_f32 v10, v4, v5
	v_cvt_pk_f16_f32 v11, v6, v7
	v_lshl_add_u64 v[4:5], s[6:7], 0, v[36:37]
	s_andn2_b64 vcc, exec, s[8:9]
	global_store_dwordx4 v[38:39], v[28:31], off sc1
	global_store_dwordx4 v[16:17], v[20:23], off sc1
	global_store_dwordx4 v[4:5], v[8:11], off sc1
	s_cbranch_vccnz .LBB0_5
	v_lshl_add_u64 v[4:5], v[32:33], 1, s[6:7]
	v_add_co_u32_e32 v4, vcc, 0x800000, v4
	v_cvt_pk_f16_f32 v0, v35, v1
	v_cvt_pk_f16_f32 v1, v2, v3
	v_cvt_pk_f16_f32 v2, v12, v13
	v_cvt_pk_f16_f32 v3, v14, v15
	v_addc_co_u32_e32 v5, vcc, 0, v5, vcc
	global_store_dwordx4 v[4:5], v[0:3], off sc1
.LBB0_5:
	s_endpgm
.Lprep_rope:
	v_lshlrev_b32_e32 v0, 1, v0
	v_and_b32_e32 v0, 62, v0
	v_cvt_f32_ubyte0_e32 v0, v0
	v_mul_f32_e32 v3, 0x3c800000, v0
	v_mov_b32_e32 v0, 0x461c4000
	v_cmp_eq_f32_e32 vcc, 0, v3
	v_lshl_or_b32 v2, v5, 8, v4
	s_load_dwordx2 s[2:3], s[0:1], 0x10
	s_load_dwordx4 s[4:7], s[0:1], 0x28
	v_cndmask_b32_e64 v5, v0, 1.0, vcc
	v_frexp_mant_f32_e32 v0, v5
	s_mov_b32 s0, 0x3f2aaaab
	v_cmp_gt_f32_e32 vcc, s0, v0
	s_mov_b32 s0, 0x3f317218
	v_ashrrev_i32_e32 v4, 5, v2
	v_cndmask_b32_e64 v1, 1.0, 2.0, vcc
	v_mul_f32_e32 v0, v0, v1
	v_add_f32_e32 v7, 1.0, v0
	v_rcp_f32_e32 v12, v7
	v_add_f32_e32 v1, -1.0, v7
	v_sub_f32_e32 v9, v0, v1
	v_add_f32_e32 v1, -1.0, v0
	v_mul_f32_e32 v13, v1, v12
	v_mul_f32_e32 v6, v7, v13
	v_fma_f32 v8, v13, v7, -v6
	v_fmac_f32_e32 v8, v13, v9
	v_add_f32_e32 v0, v6, v8
	v_sub_f32_e32 v7, v1, v0
	v_pk_add_f32 v[10:11], v[0:1], v[6:7] neg_lo:[0,1] neg_hi:[0,1]
	v_mov_b32_e32 v9, v0
	v_pk_add_f32 v[0:1], v[10:11], v[8:9] neg_lo:[0,1] neg_hi:[0,1]
	v_mov_b32_e32 v8, 0x3e91f4c4
	v_add_f32_e32 v0, v0, v1
	v_add_f32_e32 v0, v7, v0
	v_mul_f32_e32 v0, v12, v0
	v_add_f32_e32 v6, v13, v0
	v_sub_f32_e32 v1, v6, v13
	v_sub_f32_e32 v14, v0, v1
	v_mul_f32_e32 v1, v6, v6
	v_fma_f32 v7, v6, v6, -v1
	v_add_f32_e32 v0, v14, v14
	v_fmac_f32_e32 v7, v6, v0
	v_add_f32_e32 v0, v1, v7
	v_fmac_f32_e32 v8, 0x3e76c4e1, v0
	v_fmaak_f32 v8, v0, v8, 0x3ecccdef
	v_sub_f32_e32 v1, v0, v1
	v_sub_f32_e32 v15, v7, v1
	v_mul_f32_e32 v1, v0, v8
	v_fma_f32 v7, v0, v8, -v1
	v_fmac_f32_e32 v7, v15, v8
	v_add_f32_e32 v8, v1, v7
	v_sub_f32_e32 v1, v8, v1
	v_add_f32_e32 v9, 0x3f2aaaaa, v8
	v_sub_f32_e32 v1, v7, v1
	v_add_f32_e32 v7, 0x31739010, v1
	v_add_f32_e32 v1, 0xbf2aaaaa, v9
	v_sub_f32_e32 v1, v8, v1
	v_pk_mul_f32 v[10:11], v[6:7], v[0:1]
	v_pk_add_f32 v[12:13], v[6:7], v[0:1]
	v_fma_f32 v8, v0, v6, -v10
	v_fmac_f32_e32 v8, v0, v14
	v_mov_b32_e32 v11, v13
	v_fmac_f32_e32 v8, v15, v6
	v_pk_add_f32 v[0:1], v[10:11], v[8:9]
	s_mov_b32 s1, 0x42b17218
	v_sub_f32_e32 v7, v0, v10
	v_sub_f32_e32 v7, v8, v7
	v_sub_f32_e32 v8, v9, v1
	v_add_f32_e32 v11, v13, v8
	v_cvt_f64_f32_e32 v[12:13], v5
	v_frexp_exp_i32_f64_e32 v5, v[12:13]
	v_subbrev_co_u32_e32 v5, vcc, 0, v5, vcc
	v_cvt_f32_i32_e32 v5, v5
	v_pk_mul_f32 v[8:9], v[0:1], v[0:1] op_sel:[0,1] op_sel_hi:[1,0]
	v_ldexp_f32 v13, v6, 1
	v_fma_f32 v10, v0, v1, -v8
	v_fmac_f32_e32 v10, v0, v11
	v_mul_f32_e32 v0, 0x3f317218, v5
	v_fmac_f32_e32 v10, v7, v1
	v_fma_f32 v1, v5, s0, -v0
	v_fmamk_f32 v12, v5, 0xb102e308, v1
	v_add_f32_e32 v1, v8, v10
	v_pk_add_f32 v[6:7], v[0:1], v[12:13]
	v_ldexp_f32 v5, v14, 1
	v_mov_b32_e32 v14, v1
	v_mov_b32_e32 v15, v7
	v_mov_b32_e32 v9, v13
	v_pk_add_f32 v[8:9], v[14:15], v[8:9] neg_lo:[0,1] neg_hi:[0,1]
	v_mov_b32_e32 v11, v1
	v_pk_add_f32 v[8:9], v[10:11], v[8:9] neg_lo:[0,1] neg_hi:[0,1]
	v_mov_b32_e32 v13, v6
	v_add_f32_e32 v1, v5, v8
	v_ashrrev_i32_e32 v5, 31, v4
	s_waitcnt lgkmcnt(0)
	v_lshl_add_u64 v[4:5], v[4:5], 2, s[2:3]
	global_load_dword v16, v[4:5], off
	v_add_f32_e32 v1, v1, v9
	v_pk_add_f32 v[8:9], v[6:7], v[0:1] neg_lo:[0,1] neg_hi:[0,1]
	v_pk_add_f32 v[10:11], v[6:7], v[0:1]
	v_mov_b32_e32 v0, v1
	v_mov_b32_e32 v9, v11
	v_pk_add_f32 v[14:15], v[12:13], v[8:9] neg_lo:[0,1] neg_hi:[0,1]
	v_pk_add_f32 v[8:9], v[12:13], v[8:9]
	v_mov_b32_e32 v1, v6
	v_pk_add_f32 v[4:5], v[8:9], v[6:7] op_sel:[1,0] op_sel_hi:[0,1] neg_lo:[0,1] neg_hi:[0,1]
	v_pk_add_f32 v[12:13], v[10:11], v[4:5] op_sel_hi:[1,0] neg_lo:[0,1] neg_hi:[0,1]
	v_mov_b32_e32 v10, v11
	v_mov_b32_e32 v11, v9
	v_pk_mov_b32 v[4:5], v[6:7], v[4:5] op_sel:[1,0]
	v_mov_b32_e32 v12, v14
	v_pk_add_f32 v[4:5], v[10:11], v[4:5] neg_lo:[0,1] neg_hi:[0,1]
	v_mov_b32_e32 v15, v9
	v_pk_add_f32 v[0:1], v[0:1], v[4:5] neg_lo:[0,1] neg_hi:[0,1]
	s_movk_i32 s0, 0x204
	v_pk_add_f32 v[4:5], v[12:13], v[0:1]
	s_mov_b32 s3, 0x3fb8aa3b
	v_pk_add_f32 v[6:7], v[4:5], v[4:5] op_sel:[0,1] op_sel_hi:[1,0]
	s_mov_b32 s2, 0x7f800000
	v_pk_add_f32 v[8:9], v[8:9], v[6:7] op_sel:[1,0] op_sel_hi:[0,1]
	v_mov_b32_e32 v5, v8
	v_pk_add_f32 v[10:11], v[4:5], v[14:15] neg_lo:[0,1] neg_hi:[0,1]
	v_mov_b32_e32 v1, v6
	v_sub_f32_e32 v4, v4, v10
	v_pk_add_f32 v[0:1], v[0:1], v[10:11] neg_lo:[0,1] neg_hi:[0,1]
	v_sub_f32_e32 v4, v14, v4
	v_add_f32_e32 v0, v0, v4
	v_add_f32_e32 v0, v0, v1
	v_add_f32_e32 v1, v8, v0
	v_sub_f32_e32 v4, v1, v8
	v_sub_f32_e32 v0, v0, v4
	v_mul_f32_e32 v4, v3, v1
	v_fma_f32 v1, v3, v1, -v4
	v_fmac_f32_e32 v1, v3, v0
	v_add_f32_e32 v0, v4, v1
	v_cmp_class_f32_e64 vcc, v4, s0
	v_sub_f32_e32 v5, v0, v4
	v_sub_f32_e32 v1, v1, v5
	v_cndmask_b32_e32 v0, v0, v4, vcc
	v_mov_b32_e32 v4, 0x37000000
	v_cmp_eq_f32_e32 vcc, s1, v0
	v_mov_b32_e32 v9, 0x3e5ae645
	s_nop 0
	v_cndmask_b32_e32 v4, 0, v4, vcc
	v_sub_f32_e32 v5, v0, v4
	v_mul_f32_e32 v6, 0x3fb8aa3b, v5
	v_fma_f32 v7, v5, s3, -v6
	v_rndne_f32_e32 v8, v6
	v_fmamk_f32 v7, v5, 0x32a5705f, v7
	v_sub_f32_e32 v6, v6, v8
	v_add_f32_e32 v6, v6, v7
	v_exp_f32_e32 v6, v6
	v_cvt_i32_f32_e32 v7, v8
	v_cmp_neq_f32_e64 vcc, |v0|, s2
	s_mov_b32 s3, 0xc2ce8ed0
	v_mov_b32_e32 v8, 0x67f544e4
	v_cndmask_b32_e32 v0, 0, v1, vcc
	v_ldexp_f32 v1, v6, v7
	v_cmp_ngt_f32_e32 vcc, s3, v5
	v_add_f32_e32 v0, v4, v0
	v_mov_b32_e32 v4, 0x7f800000
	v_cndmask_b32_e32 v1, 0, v1, vcc
	v_cmp_nlt_f32_e32 vcc, s1, v5
	s_nop 1
	v_cndmask_b32_e32 v1, v4, v1, vcc
	v_fma_f32 v0, v1, v0, v1
	v_cmp_class_f32_e64 vcc, v1, s0
	s_nop 1
	v_cndmask_b32_e32 v0, v0, v1, vcc
	v_and_b32_e32 v1, 0x7fffffff, v0
	v_div_scale_f32 v4, s[0:1], v1, v1, 1.0
	v_rcp_f32_e32 v5, v4
	v_div_scale_f32 v1, vcc, 1.0, v1, 1.0
	s_mov_b32 s0, 0x6dc9c883
	v_fma_f32 v6, -v4, v5, 1.0
	v_fmac_f32_e32 v5, v6, v5
	v_mul_f32_e32 v6, v1, v5
	v_fma_f32 v7, -v4, v6, v1
	v_fmac_f32_e32 v6, v7, v5
	v_fma_f32 v1, -v4, v6, v1
	s_waitcnt vmcnt(0)
	v_cvt_f32_i32_e32 v4, v16
	v_div_fmas_f32 v1, v1, v5, v6
	v_div_fixup_f32 v0, v1, |v0|, 1.0
	v_cmp_neq_f32_e32 vcc, s2, v3
	s_mov_b32 s1, 0x3fc45f30
	v_mov_b32_e32 v6, 0x13a86d09
	v_cndmask_b32_e32 v0, 0, v0, vcc
	v_mul_f32_e32 v0, v0, v4
	v_cvt_f64_f32_e32 v[0:1], v0
	v_mul_f64 v[4:5], v[0:1], s[0:1]
	v_rndne_f64_e32 v[4:5], v[4:5]
	v_fma_f64 v[0:1], v[0:1], s[0:1], -v[4:5]
	s_mov_b32 s0, 0x54442d18
	s_mov_b32 s1, 0x3ff921fb
	v_mul_f64 v[0:1], v[0:1], s[0:1]
	s_mov_b32 s0, 0xe733b81f
	v_mul_f64 v[4:5], v[0:1], v[0:1]
	v_mov_b32_e32 v7, 0xbde61246
	s_mov_b32 s1, 0x3d6ae7f3
	v_fmac_f64_e32 v[6:7], s[0:1], v[4:5]
	v_fmac_f64_e32 v[8:9], v[4:5], v[6:7]
	v_mov_b32_e32 v6, 0xa556c734
	v_mov_b32_e32 v7, 0xbec71de3
	v_fmac_f64_e32 v[6:7], v[4:5], v[8:9]
	v_mov_b32_e32 v8, 0x1a01a01a
	v_mov_b32_e32 v9, 0x3f2a01a0
	v_mov_b64_e32 v[10:11], v[8:9]
	v_fmac_f64_e32 v[10:11], v[4:5], v[6:7]
	v_mov_b32_e32 v6, 0x11111111
	v_mov_b32_e32 v7, 0xbf811111
	v_fmac_f64_e32 v[6:7], v[4:5], v[10:11]
	v_mov_b32_e32 v10, 0x55555555
	v_mov_b32_e32 v11, 0x3fc55555
	v_mov_b64_e32 v[12:13], v[10:11]
	v_fmac_f64_e32 v[12:13], v[4:5], v[6:7]
	v_mul_f64 v[6:7], v[0:1], v[4:5]
	s_mov_b32 s0, 0xa8c07c9d
	v_fma_f64 v[0:1], -v[6:7], v[12:13], v[0:1]
	v_mov_b32_e32 v6, 0xeff8d898
	v_mov_b32_e32 v7, 0xbe21eed8
	s_mov_b32 s1, 0x3da93974
	v_fmac_f64_e32 v[6:7], s[0:1], v[4:5]
	v_mov_b32_e32 v12, 0xb7789f5c
	v_mov_b32_e32 v13, 0x3e927e4f
	v_fmac_f64_e32 v[12:13], v[4:5], v[6:7]
	v_mov_b32_e32 v9, 0xbefa01a0
	v_fmac_f64_e32 v[8:9], v[4:5], v[12:13]
	v_mov_b32_e32 v6, 0x16c16c17
	v_mov_b32_e32 v7, 0x3f56c16c
	v_fmac_f64_e32 v[6:7], v[4:5], v[8:9]
	v_mov_b32_e32 v11, 0xbfa55555
	v_fmac_f64_e32 v[10:11], v[4:5], v[6:7]
	v_fma_f64 v[6:7], v[4:5], v[10:11], 0.5
	v_fma_f64 v[4:5], -v[4:5], v[6:7], 1.0
	v_add_f64 v[6:7], v[0:1], v[0:1]
	v_mul_f64 v[4:5], v[4:5], v[6:7]
	v_fma_f64 v[0:1], -v[0:1], v[6:7], 1.0
	v_add_f64 v[6:7], v[4:5], v[4:5]
	v_ashrrev_i32_e32 v3, 31, v2
	v_fma_f64 v[4:5], -v[4:5], v[6:7], 1.0
	v_lshlrev_b64 v[2:3], 2, v[2:3]
	v_mul_f64 v[0:1], v[6:7], v[0:1]
	v_cvt_f32_f64_e32 v6, v[4:5]
	v_lshl_add_u64 v[4:5], s[4:5], 0, v[2:3]
	global_store_dword v[4:5], v6, off
	v_cvt_f32_f64_e32 v4, v[0:1]
	v_lshl_add_u64 v[0:1], s[6:7], 0, v[2:3]
	global_store_dword v[0:1], v4, off
